# NA attention units remapped so the 8 waves of a workgroup share one head and cover 8 adjacent grid rows (L1 reuse of K/V)
# speedup vs baseline: 1.0069x; 1.0069x over previous
.LBB0_866:
	s_cmpk_gt_i32 s8, 0x7ff
	s_cselect_b64 s[24:25], -1, 0
	s_cmpk_lt_i32 s8, 0x800
	s_cselect_b64 s[2:3], -1, 0
	s_mov_b64 s[4:5], -1
	s_and_b64 vcc, exec, s[24:25]
	s_cbranch_vccnz .LBB0_869
	s_ashr_i32 s6, s8, 9
	s_and_b32 s7, s8, 31
	s_lshl_b32 s4, s6, 11
	s_lshl_b32 s5, s7, 6
	s_or_b32 s9, s5, s4
	s_cbranch_execz .LBB0_870
.LBB0_868:
	s_bfe_u32 s4, s8, 0x40005
	s_andn2_b64 vcc, exec, s[2:3]
	s_mov_b32 s31, 8
	s_cbranch_vccz .LBB0_871
	s_branch .LBB0_874
